# dense attention: 4-slot K/V LDS ring, one barrier per tile, scale+exp of new scores merged under the PV MFMAs
# speedup vs baseline: 1.0178x; 1.0063x over previous
.LBB0_409:
	s_waitcnt vmcnt(0)
	v_mov_b32_e32 v254, v116
	v_mov_b32_e32 v255, v118
	ds_write_b64 v189, v[254:255] offset:8192
	v_mov_b32_e32 v244, v117
	v_mov_b32_e32 v245, v119
	ds_write_b64 v190, v[244:245] offset:8192
	ds_write_b128 v191, v[120:123] offset:40960
	ds_read_b128 v[200:203], v192 offset:53248
	ds_read_b128 v[68:71], v192 offset:49152
	ds_read_b128 v[72:75], v193 offset:49152
	ds_read_b128 v[204:207], v193 offset:53248
	v_add_u32_e32 v252, 0xffffe000, v152
	v_mov_b32_e32 v253, v3
	v_lshl_add_u64 v[252:253], v[148:149], 0, v[252:253]
	v_cvt_pk_fp8_f32 v232, v173, v177
	v_cvt_pk_fp8_f32 v233, v174, v178
	v_cvt_pk_fp8_f32 v234, v175, v179
	v_cvt_pk_fp8_f32 v235, v176, v180
	v_cvt_pk_fp8_f32 v232, v165, v166 op_sel:[0,0,1]
	v_cvt_pk_fp8_f32 v233, v167, v168 op_sel:[0,0,1]
	v_cvt_pk_fp8_f32 v234, v169, v170 op_sel:[0,0,1]
	v_cvt_pk_fp8_f32 v235, v171, v172 op_sel:[0,0,1]
	v_exp_f32_e32 v154, v154
	v_add_f32_e32 v240, v173, v177
	v_exp_f32_e32 v155, v155
	v_add_f32_e32 v240, v165, v240
	v_exp_f32_e32 v130, v130
	s_waitcnt lgkmcnt(1)
	v_mfma_scale_f32_32x32x64_f8f6f4 v[84:99], v[68:75], v[100:107], 0, v188, v188 op_sel_hi:[0,0,0]
	v_add_f32_e32 v240, v166, v240
	v_exp_f32_e32 v131, v131
	v_add_f32_e32 v240, v174, v240
	v_exp_f32_e32 v128, v128
	v_add_f32_e32 v240, v178, v240
	v_exp_f32_e32 v129, v129
	v_add_f32_e32 v240, v167, v240
	v_exp_f32_e32 v126, v126
	v_add_f32_e32 v240, v168, v240
	v_exp_f32_e32 v127, v127
	v_add_f32_e32 v240, v175, v240
	v_exp_f32_e32 v124, v124
	v_add_f32_e32 v240, v179, v240
	v_exp_f32_e32 v125, v125
	v_add_f32_e32 v240, v169, v240
	v_exp_f32_e32 v160, v160
	s_waitcnt lgkmcnt(0)
	v_mfma_scale_f32_32x32x64_f8f6f4 v[68:83], v[200:207], v[100:107], 0, v188, v188 op_sel_hi:[0,0,0]
	ds_read_b128 v[200:203], v194 offset:53248
	ds_read_b128 v[208:211], v194 offset:49152
	ds_read_b128 v[212:215], v195 offset:49152
	ds_read_b128 v[204:207], v195 offset:53248
	v_add_f32_e32 v240, v170, v240
	v_exp_f32_e32 v161, v161
	v_add_f32_e32 v240, v176, v240
	v_exp_f32_e32 v158, v158
	v_add_f32_e32 v240, v180, v240
	v_exp_f32_e32 v159, v159
	v_add_f32_e32 v240, v171, v240
	v_exp_f32_e32 v156, v156
	v_add_f32_e32 v240, v172, v240
	v_exp_f32_e32 v157, v157
	v_cvt_pk_fp8_f32 v236, v154, v155
	v_cvt_pk_fp8_f32 v237, v128, v129
	v_cvt_pk_fp8_f32 v238, v124, v125
	v_cvt_pk_fp8_f32 v239, v158, v159
	v_cvt_pk_fp8_f32 v236, v130, v131 op_sel:[0,0,1]
	v_cvt_pk_fp8_f32 v237, v126, v127 op_sel:[0,0,1]
	s_waitcnt lgkmcnt(1)
	v_mfma_scale_f32_32x32x64_f8f6f4 v[84:99], v[208:215], v[108:115], v[84:99], v188, v188 op_sel_hi:[0,0,0]
	v_cvt_pk_fp8_f32 v238, v160, v161 op_sel:[0,0,1]
	v_cvt_pk_fp8_f32 v239, v156, v157 op_sel:[0,0,1]
	v_add_f32_e32 v241, v128, v129
	v_add_f32_e32 v241, v124, v241
	v_add_f32_e32 v241, v125, v241
	v_add_f32_e32 v241, v126, v241
	v_add_f32_e32 v241, v127, v241
	v_add_f32_e32 v241, v130, v241
	v_add_f32_e32 v241, v131, v241
	v_add_f32_e32 v241, v154, v241
	v_add_f32_e32 v241, v155, v241
	v_add_f32_e32 v241, v160, v241
	v_add_f32_e32 v241, v161, v241
	v_add_f32_e32 v241, v158, v241
	v_add_f32_e32 v241, v159, v241
	v_add_f32_e32 v241, v156, v241
	s_waitcnt lgkmcnt(0)
	v_mfma_scale_f32_32x32x64_f8f6f4 v[68:83], v[200:207], v[108:115], v[68:83], v188, v188 op_sel_hi:[0,0,0]
	ds_read_b128 v[200:203], v197
	ds_read_b128 v[204:207], v198
	ds_read_b128 v[208:211], v197 offset:2048
	ds_read_b128 v[212:215], v198 offset:2048
	ds_read_b128 v[216:219], v197 offset:4096
	ds_read_b128 v[220:223], v198 offset:4096
	ds_read_b128 v[224:227], v197 offset:6144
	ds_read_b128 v[228:231], v198 offset:6144
	global_load_dwordx4 v[124:127], v[150:151], off offset:-64
	global_load_dwordx4 v[128:131], v[252:253], off
	v_add_f32_e32 v241, v157, v241
	v_add_f32_e32 v162, v240, v241
	v_mov_b32_e32 v163, v162
	s_nop 0
	s_nop 0
	v_permlane32_swap_b32_e32 v162, v163
	v_max3_f32 v246, v84, v85, v86
	v_max3_f32 v246, v246, v87, v88
	v_max3_f32 v246, v246, v89, v90
	v_max3_f32 v246, v246, v91, v92
	v_max3_f32 v246, v246, v93, v94
	v_max3_f32 v246, v246, v95, v96
	v_max3_f32 v246, v246, v97, v98
	v_max_f32_e32 v246, v246, v99
	v_max3_f32 v248, v68, v69, v70
	v_max3_f32 v248, v248, v71, v72
	v_max3_f32 v248, v248, v73, v74
	v_max3_f32 v248, v248, v75, v76
	v_max3_f32 v248, v248, v77, v78
	s_waitcnt lgkmcnt(6)
	v_mfma_scale_f32_32x32x64_f8f6f4 v[52:67], v[232:239], v[200:207], v[52:67], v188, v188 op_sel_hi:[0,0,0]
	v_max3_f32 v248, v248, v79, v80
	v_max3_f32 v248, v248, v81, v82
	v_max_f32_e32 v248, v248, v83
	v_max_f32_e32 v250, v246, v248
	v_mov_b32_e32 v251, v250
	s_nop 0
	s_nop 0
	v_permlane32_swap_b32_e32 v250, v251
	v_max_f32_e32 v250, v250, v251
	v_sub_f32_e32 v154, v250, v153
	v_max_f32_e32 v2, v153, v250
	v_sub_f32_e32 v155, v153, v2
	v_mul_f32_e32 v155, 0x3e0293ee, v155
	v_exp_f32_e32 v155, v155
	v_cmp_ge_f32_e32 vcc, s55, v154
	s_cmp_eq_u64 vcc, exec
	s_cselect_b64 s[4:5], -1, 0
	v_cndmask_b32_e64 v164, v155, 1.0, s[4:5]
	v_cmp_gt_f32_e32 vcc, 1.0, v164
	s_waitcnt lgkmcnt(4)
	v_mfma_scale_f32_32x32x64_f8f6f4 v[36:51], v[232:239], v[208:215], v[36:51], v188, v188 op_sel_hi:[0,0,0]
	v_cndmask_b32_e64 v154, v2, v153, s[4:5]
	v_mul_f32_e32 v247, 0xbe0293ee, v154
	v_fmamk_f32 v84, v84, 0x3e0293ee, v247
	v_exp_f32_e32 v165, v84
	v_fmamk_f32 v85, v85, 0x3e0293ee, v247
	v_exp_f32_e32 v169, v85
	v_fmamk_f32 v86, v86, 0x3e0293ee, v247
	v_exp_f32_e32 v2, v86
	v_fmamk_f32 v87, v87, 0x3e0293ee, v247
	v_exp_f32_e32 v155, v87
	v_fmamk_f32 v88, v88, 0x3e0293ee, v247
	v_exp_f32_e32 v166, v88
	v_fmamk_f32 v89, v89, 0x3e0293ee, v247
	v_exp_f32_e32 v170, v89
	v_fmamk_f32 v90, v90, 0x3e0293ee, v247
	v_exp_f32_e32 v156, v90
	v_fmamk_f32 v91, v91, 0x3e0293ee, v247
	s_waitcnt lgkmcnt(2)
	v_mfma_scale_f32_32x32x64_f8f6f4 v[20:35], v[232:239], v[216:223], v[20:35], v188, v188 op_sel_hi:[0,0,0]
	v_exp_f32_e32 v157, v91
	v_fmamk_f32 v92, v92, 0x3e0293ee, v247
	v_exp_f32_e32 v167, v92
	v_fmamk_f32 v93, v93, 0x3e0293ee, v247
	v_exp_f32_e32 v171, v93
	v_fmamk_f32 v94, v94, 0x3e0293ee, v247
	v_exp_f32_e32 v158, v94
	v_fmamk_f32 v95, v95, 0x3e0293ee, v247
	v_exp_f32_e32 v159, v95
	v_fmamk_f32 v96, v96, 0x3e0293ee, v247
	v_exp_f32_e32 v168, v96
	v_fmamk_f32 v97, v97, 0x3e0293ee, v247
	v_exp_f32_e32 v172, v97
	v_fmamk_f32 v98, v98, 0x3e0293ee, v247
	v_exp_f32_e32 v160, v98
	v_fmamk_f32 v99, v99, 0x3e0293ee, v247
	v_exp_f32_e32 v161, v99
	s_waitcnt lgkmcnt(0)
	v_mfma_scale_f32_32x32x64_f8f6f4 v[4:19], v[232:239], v[224:231], v[4:19], v188, v188 op_sel_hi:[0,0,0]
	v_fmamk_f32 v173, v68, 0x3e0293ee, v247
	v_fmamk_f32 v174, v69, 0x3e0293ee, v247
	v_fmamk_f32 v175, v70, 0x3e0293ee, v247
	v_fmamk_f32 v176, v71, 0x3e0293ee, v247
	v_fmamk_f32 v177, v72, 0x3e0293ee, v247
	v_fmamk_f32 v178, v73, 0x3e0293ee, v247
	v_fmamk_f32 v179, v74, 0x3e0293ee, v247
	v_fmamk_f32 v180, v75, 0x3e0293ee, v247
	v_fmamk_f32 v181, v76, 0x3e0293ee, v247
	v_fmamk_f32 v182, v77, 0x3e0293ee, v247
	v_fmamk_f32 v183, v78, 0x3e0293ee, v247
	v_fmamk_f32 v200, v79, 0x3e0293ee, v247
	v_fmamk_f32 v201, v80, 0x3e0293ee, v247
	v_fmamk_f32 v208, v81, 0x3e0293ee, v247
	v_fmamk_f32 v209, v82, 0x3e0293ee, v247
	v_fmamk_f32 v153, v83, 0x3e0293ee, v247
	s_cbranch_vccz .Lring_noresc_a0
	s_nop 15
	s_nop 7
	s_and_saveexec_b64 s[8:9], s[6:7]
	ds_write_b32 v184, v164 offset:128
	s_or_b64 exec, exec, s[8:9]
	s_waitcnt lgkmcnt(0)
	v_add_u32_e32 v228, v135, v185
	ds_read_b128 v[224:227], v228 offset:224
	ds_read_b128 v[220:223], v228 offset:192
	ds_read_b128 v[216:219], v228 offset:160
	ds_read_b128 v[212:215], v228 offset:128
	s_waitcnt lgkmcnt(0)
	v_pk_mul_f32 v[52:53], v[52:53], v[212:213]
	v_pk_mul_f32 v[54:55], v[54:55], v[214:215]
	v_pk_mul_f32 v[56:57], v[56:57], v[216:217]
	v_pk_mul_f32 v[58:59], v[58:59], v[218:219]
	v_pk_mul_f32 v[60:61], v[60:61], v[220:221]
	v_pk_mul_f32 v[62:63], v[62:63], v[222:223]
	v_pk_mul_f32 v[64:65], v[64:65], v[224:225]
	v_pk_mul_f32 v[66:67], v[66:67], v[226:227]
	v_pk_mul_f32 v[36:37], v[36:37], v[212:213]
	v_pk_mul_f32 v[38:39], v[38:39], v[214:215]
	v_pk_mul_f32 v[40:41], v[40:41], v[216:217]
	v_pk_mul_f32 v[42:43], v[42:43], v[218:219]
	v_pk_mul_f32 v[44:45], v[44:45], v[220:221]
	v_pk_mul_f32 v[46:47], v[46:47], v[222:223]
	v_pk_mul_f32 v[48:49], v[48:49], v[224:225]
	v_pk_mul_f32 v[50:51], v[50:51], v[226:227]
	v_pk_mul_f32 v[20:21], v[20:21], v[212:213]
	v_pk_mul_f32 v[22:23], v[22:23], v[214:215]
	v_pk_mul_f32 v[24:25], v[24:25], v[216:217]
	v_pk_mul_f32 v[26:27], v[26:27], v[218:219]
	v_pk_mul_f32 v[28:29], v[28:29], v[220:221]
	v_pk_mul_f32 v[30:31], v[30:31], v[222:223]
	v_pk_mul_f32 v[32:33], v[32:33], v[224:225]
	v_pk_mul_f32 v[34:35], v[34:35], v[226:227]
	v_pk_mul_f32 v[4:5], v[4:5], v[212:213]
	v_pk_mul_f32 v[6:7], v[6:7], v[214:215]
	v_pk_mul_f32 v[8:9], v[8:9], v[216:217]
	v_pk_mul_f32 v[10:11], v[10:11], v[218:219]
	v_pk_mul_f32 v[12:13], v[12:13], v[220:221]
	v_pk_mul_f32 v[14:15], v[14:15], v[222:223]
	v_pk_mul_f32 v[16:17], v[16:17], v[224:225]
	v_pk_mul_f32 v[18:19], v[18:19], v[226:227]
.Lring_noresc_a0:
	s_waitcnt lgkmcnt(0)
	s_barrier
	s_waitcnt vmcnt(0)
	v_mov_b32_e32 v254, v124
	v_mov_b32_e32 v255, v126
	ds_write_b64 v189, v[254:255] offset:24576
	v_mov_b32_e32 v244, v125
	v_mov_b32_e32 v245, v127
	ds_write_b64 v190, v[244:245] offset:24576
	ds_write_b128 v191, v[128:131] offset:57344
	s_cmp_gt_u32 s15, 60
	s_cselect_b64 s[8:9], -1, 0
	s_and_b64 vcc, exec, s[8:9]
	s_cbranch_vccnz .Lring_noload_b0
	v_mov_b32_e32 v252, v152
	v_mov_b32_e32 v253, v3
	v_lshl_add_u64 v[120:121], v[148:149], 0, v[252:253]
	global_load_dwordx4 v[116:119], v[150:151], off
	s_nop 0
	global_load_dwordx4 v[120:123], v[120:121], off
.Lring_noload_b0:
	ds_read_b128 v[210:213], v192 offset:45056
	ds_read_b128 v[68:71], v192 offset:40960
	ds_read_b128 v[72:75], v193 offset:40960
	ds_read_b128 v[214:217], v193 offset:45056
	v_cvt_pk_fp8_f32 v232, v165, v169
	v_cvt_pk_fp8_f32 v233, v166, v170
	v_cvt_pk_fp8_f32 v234, v167, v171
	v_cvt_pk_fp8_f32 v235, v168, v172
	v_cvt_pk_fp8_f32 v232, v2, v155 op_sel:[0,0,1]
	v_cvt_pk_fp8_f32 v233, v156, v157 op_sel:[0,0,1]
	v_cvt_pk_fp8_f32 v234, v158, v159 op_sel:[0,0,1]
	v_cvt_pk_fp8_f32 v235, v160, v161 op_sel:[0,0,1]
	v_exp_f32_e32 v173, v173
	v_add_f32_e32 v240, v165, v169
	v_exp_f32_e32 v174, v174
	v_add_f32_e32 v240, v2, v240
	v_exp_f32_e32 v175, v175
	v_add_f32_e32 v240, v155, v240
	v_exp_f32_e32 v176, v176
	v_add_f32_e32 v240, v166, v240
	s_waitcnt lgkmcnt(1)
	v_mfma_scale_f32_32x32x64_f8f6f4 v[84:99], v[68:75], v[100:107], 0, v188, v188 op_sel_hi:[0,0,0]
	v_exp_f32_e32 v177, v177
	v_add_f32_e32 v240, v170, v240
	v_exp_f32_e32 v178, v178
	v_add_f32_e32 v240, v156, v240
	v_exp_f32_e32 v179, v179
	v_add_f32_e32 v240, v157, v240
	v_exp_f32_e32 v180, v180
	v_add_f32_e32 v240, v167, v240
	v_exp_f32_e32 v181, v181
	v_add_f32_e32 v240, v171, v240
	v_exp_f32_e32 v182, v182
	v_add_f32_e32 v240, v158, v240
	v_exp_f32_e32 v183, v183
	v_add_f32_e32 v240, v159, v240
	v_exp_f32_e32 v200, v200
	v_add_f32_e32 v240, v168, v240
	s_waitcnt lgkmcnt(0)
	v_mfma_scale_f32_32x32x64_f8f6f4 v[68:83], v[210:217], v[100:107], 0, v188, v188 op_sel_hi:[0,0,0]
	ds_read_b128 v[210:213], v194 offset:45056
	ds_read_b128 v[218:221], v194 offset:40960
	ds_read_b128 v[222:225], v195 offset:40960
	ds_read_b128 v[214:217], v195 offset:45056
	v_exp_f32_e32 v201, v201
	v_add_f32_e32 v240, v172, v240
	v_exp_f32_e32 v208, v208
	v_add_f32_e32 v240, v160, v240
	v_exp_f32_e32 v209, v209
	v_add_f32_e32 v240, v161, v240
	v_exp_f32_e32 v153, v153
	v_cvt_pk_fp8_f32 v236, v173, v174
	v_cvt_pk_fp8_f32 v237, v177, v178
	v_cvt_pk_fp8_f32 v238, v181, v182
	v_cvt_pk_fp8_f32 v239, v201, v208
	v_cvt_pk_fp8_f32 v236, v175, v176 op_sel:[0,0,1]
	v_cvt_pk_fp8_f32 v237, v179, v180 op_sel:[0,0,1]
	v_cvt_pk_fp8_f32 v238, v183, v200 op_sel:[0,0,1]
	v_cvt_pk_fp8_f32 v239, v209, v153 op_sel:[0,0,1]
	v_add_f32_e32 v241, v173, v200
	s_waitcnt lgkmcnt(1)
	v_mfma_scale_f32_32x32x64_f8f6f4 v[84:99], v[218:225], v[108:115], v[84:99], v188, v188 op_sel_hi:[0,0,0]
	v_add_f32_e32 v241, v201, v241
	v_add_f32_e32 v241, v174, v241
	v_add_f32_e32 v241, v175, v241
	v_add_f32_e32 v241, v176, v241
	v_add_f32_e32 v241, v177, v241
	v_add_f32_e32 v241, v178, v241
	v_add_f32_e32 v241, v179, v241
	v_add_f32_e32 v241, v180, v241
	v_add_f32_e32 v241, v181, v241
	v_add_f32_e32 v241, v182, v241
	v_add_f32_e32 v241, v183, v241
	v_add_f32_e32 v241, v208, v241
	v_add_f32_e32 v241, v209, v241
	v_add_f32_e32 v241, v153, v241
	v_add_f32_e32 v181, v240, v241
	v_mov_b32_e32 v182, v181
	s_nop 0
	s_nop 0
	v_permlane32_swap_b32_e32 v181, v182
	s_waitcnt lgkmcnt(0)
	v_mfma_scale_f32_32x32x64_f8f6f4 v[68:83], v[210:217], v[108:115], v[68:83], v188, v188 op_sel_hi:[0,0,0]
	ds_read_b128 v[200:203], v197 offset:16384
	ds_read_b128 v[204:207], v198 offset:16384
	ds_read_b128 v[208:211], v197 offset:18432
	ds_read_b128 v[212:215], v198 offset:18432
	ds_read_b128 v[216:219], v197 offset:20480
	ds_read_b128 v[220:223], v198 offset:20480
	ds_read_b128 v[224:227], v197 offset:22528
	ds_read_b128 v[228:231], v198 offset:22528
	v_max3_f32 v246, v84, v85, v86
	v_max3_f32 v246, v246, v87, v88
	v_max3_f32 v246, v246, v89, v90
	v_max3_f32 v246, v246, v91, v92
	v_max3_f32 v246, v246, v93, v94
	v_max3_f32 v246, v246, v95, v96
	v_max3_f32 v246, v246, v97, v98
	v_max_f32_e32 v246, v246, v99
	s_nop 3
	v_max3_f32 v248, v68, v69, v70
	v_max3_f32 v248, v248, v71, v72
	v_max3_f32 v248, v248, v73, v74
	v_max3_f32 v248, v248, v75, v76
	v_max3_f32 v248, v248, v77, v78
	v_max3_f32 v248, v248, v79, v80
	v_max3_f32 v248, v248, v81, v82
	v_max_f32_e32 v248, v248, v83
	v_max_f32_e32 v250, v246, v248
	s_waitcnt lgkmcnt(6)
	v_mfma_scale_f32_32x32x64_f8f6f4 v[52:67], v[232:239], v[200:207], v[52:67], v188, v188 op_sel_hi:[0,0,0]
	v_mov_b32_e32 v251, v250
	s_nop 1
	v_permlane32_swap_b32_e32 v250, v251
	v_max_f32_e32 v250, v250, v251
	v_sub_f32_e32 v155, v250, v154
	v_max_f32_e32 v153, v154, v250
	v_sub_f32_e32 v2, v154, v153
	v_mul_f32_e32 v2, 0x3e0293ee, v2
	v_exp_f32_e32 v2, v2
	v_cmp_ge_f32_e32 vcc, s55, v155
	s_cmp_eq_u64 vcc, exec
	s_cselect_b64 s[4:5], -1, 0
	v_cndmask_b32_e64 v2, v2, 1.0, s[4:5]
	v_cmp_gt_f32_e32 vcc, 1.0, v2
	v_cndmask_b32_e64 v153, v153, v154, s[4:5]
	v_mul_f32_e32 v247, 0xbe0293ee, v153
	v_fmamk_f32 v84, v84, 0x3e0293ee, v247
	v_exp_f32_e32 v173, v84
	s_waitcnt lgkmcnt(4)
	v_mfma_scale_f32_32x32x64_f8f6f4 v[36:51], v[232:239], v[208:215], v[36:51], v188, v188 op_sel_hi:[0,0,0]
	v_fmamk_f32 v85, v85, 0x3e0293ee, v247
	v_exp_f32_e32 v177, v85
	v_fmamk_f32 v86, v86, 0x3e0293ee, v247
	v_exp_f32_e32 v165, v86
	v_fmamk_f32 v87, v87, 0x3e0293ee, v247
	v_exp_f32_e32 v166, v87
	v_fmamk_f32 v88, v88, 0x3e0293ee, v247
	v_exp_f32_e32 v174, v88
	v_fmamk_f32 v89, v89, 0x3e0293ee, v247
	v_exp_f32_e32 v178, v89
	v_fmamk_f32 v90, v90, 0x3e0293ee, v247
	v_exp_f32_e32 v167, v90
	v_fmamk_f32 v91, v91, 0x3e0293ee, v247
	v_exp_f32_e32 v168, v91
	v_fmamk_f32 v92, v92, 0x3e0293ee, v247
	v_exp_f32_e32 v175, v92
	v_fmamk_f32 v93, v93, 0x3e0293ee, v247
	s_waitcnt lgkmcnt(2)
	v_mfma_scale_f32_32x32x64_f8f6f4 v[20:35], v[232:239], v[216:223], v[20:35], v188, v188 op_sel_hi:[0,0,0]
	v_exp_f32_e32 v179, v93
	v_fmamk_f32 v94, v94, 0x3e0293ee, v247
	v_exp_f32_e32 v169, v94
	v_fmamk_f32 v95, v95, 0x3e0293ee, v247
	v_exp_f32_e32 v170, v95
	v_fmamk_f32 v96, v96, 0x3e0293ee, v247
	v_exp_f32_e32 v176, v96
	v_fmamk_f32 v97, v97, 0x3e0293ee, v247
	v_exp_f32_e32 v180, v97
	v_fmamk_f32 v98, v98, 0x3e0293ee, v247
	v_exp_f32_e32 v171, v98
	v_fmamk_f32 v99, v99, 0x3e0293ee, v247
	v_exp_f32_e32 v172, v99
	v_fmamk_f32 v154, v68, 0x3e0293ee, v247
	v_fmamk_f32 v155, v69, 0x3e0293ee, v247
	v_fmamk_f32 v130, v70, 0x3e0293ee, v247
	v_fmamk_f32 v131, v71, 0x3e0293ee, v247
	s_waitcnt lgkmcnt(0)
	v_mfma_scale_f32_32x32x64_f8f6f4 v[4:19], v[232:239], v[224:231], v[4:19], v188, v188 op_sel_hi:[0,0,0]
	v_fmamk_f32 v128, v72, 0x3e0293ee, v247
	v_fmamk_f32 v129, v73, 0x3e0293ee, v247
	v_fmamk_f32 v126, v74, 0x3e0293ee, v247
	v_fmamk_f32 v127, v75, 0x3e0293ee, v247
	v_fmamk_f32 v124, v76, 0x3e0293ee, v247
	v_fmamk_f32 v125, v77, 0x3e0293ee, v247
	v_fmamk_f32 v160, v78, 0x3e0293ee, v247
	v_fmamk_f32 v161, v79, 0x3e0293ee, v247
	v_fmamk_f32 v158, v80, 0x3e0293ee, v247
	v_fmamk_f32 v159, v81, 0x3e0293ee, v247
	v_fmamk_f32 v156, v82, 0x3e0293ee, v247
	v_fmamk_f32 v157, v83, 0x3e0293ee, v247
	v_add_f32_e32 v249, v162, v163
	v_fmac_f32_e32 v249, v147, v145
	v_add_f32_e32 v145, v181, v182
	v_fmac_f32_e32 v145, v249, v164
	s_cbranch_vccz .Lring_noresc_b0
	s_nop 15
	s_nop 7
	s_and_saveexec_b64 s[10:11], s[6:7]
	ds_write_b32 v184, v2 offset:128
	s_or_b64 exec, exec, s[10:11]
	s_waitcnt lgkmcnt(0)
	v_add_u32_e32 v228, v135, v185
	ds_read_b128 v[224:227], v228 offset:224
	ds_read_b128 v[220:223], v228 offset:192
	ds_read_b128 v[216:219], v228 offset:160
	ds_read_b128 v[212:215], v228 offset:128
	s_waitcnt lgkmcnt(0)
	v_pk_mul_f32 v[52:53], v[52:53], v[212:213]
	v_pk_mul_f32 v[54:55], v[54:55], v[214:215]
	v_pk_mul_f32 v[56:57], v[56:57], v[216:217]
	v_pk_mul_f32 v[58:59], v[58:59], v[218:219]
	v_pk_mul_f32 v[60:61], v[60:61], v[220:221]
	v_pk_mul_f32 v[62:63], v[62:63], v[222:223]
	v_pk_mul_f32 v[64:65], v[64:65], v[224:225]
	v_pk_mul_f32 v[66:67], v[66:67], v[226:227]
	v_pk_mul_f32 v[36:37], v[36:37], v[212:213]
	v_pk_mul_f32 v[38:39], v[38:39], v[214:215]
	v_pk_mul_f32 v[40:41], v[40:41], v[216:217]
	v_pk_mul_f32 v[42:43], v[42:43], v[218:219]
	v_pk_mul_f32 v[44:45], v[44:45], v[220:221]
	v_pk_mul_f32 v[46:47], v[46:47], v[222:223]
	v_pk_mul_f32 v[48:49], v[48:49], v[224:225]
	v_pk_mul_f32 v[50:51], v[50:51], v[226:227]
	v_pk_mul_f32 v[20:21], v[20:21], v[212:213]
	v_pk_mul_f32 v[22:23], v[22:23], v[214:215]
	v_pk_mul_f32 v[24:25], v[24:25], v[216:217]
	v_pk_mul_f32 v[26:27], v[26:27], v[218:219]
	v_pk_mul_f32 v[28:29], v[28:29], v[220:221]
	v_pk_mul_f32 v[30:31], v[30:31], v[222:223]
	v_pk_mul_f32 v[32:33], v[32:33], v[224:225]
	v_pk_mul_f32 v[34:35], v[34:35], v[226:227]
	v_pk_mul_f32 v[4:5], v[4:5], v[212:213]
	v_pk_mul_f32 v[6:7], v[6:7], v[214:215]
	v_pk_mul_f32 v[8:9], v[8:9], v[216:217]
	v_pk_mul_f32 v[10:11], v[10:11], v[218:219]
	v_pk_mul_f32 v[12:13], v[12:13], v[220:221]
	v_pk_mul_f32 v[14:15], v[14:15], v[222:223]
	v_pk_mul_f32 v[16:17], v[16:17], v[224:225]
	v_pk_mul_f32 v[18:19], v[18:19], v[226:227]
.Lring_noresc_b0:
	s_add_i32 s15, s15, 2
	v_lshl_add_u64 v[150:151], v[150:151], 0, s[28:29]
	v_add_u32_e32 v152, 0x4000, v152
	s_and_b64 vcc, exec, s[8:9]
	s_waitcnt lgkmcnt(0)
	s_barrier
	s_cbranch_vccnz .LBB0_421
	v_mov_b32_e32 v147, v2
	s_waitcnt vmcnt(0)
	v_mov_b32_e32 v254, v116
	v_mov_b32_e32 v255, v118
	ds_write_b64 v189, v[254:255]
	v_mov_b32_e32 v244, v117
	v_mov_b32_e32 v245, v119
	ds_write_b64 v190, v[244:245]
	ds_write_b128 v191, v[120:123] offset:32768
	ds_read_b128 v[200:203], v192 offset:61440
	ds_read_b128 v[68:71], v192 offset:57344
	ds_read_b128 v[72:75], v193 offset:57344
	ds_read_b128 v[204:207], v193 offset:61440
	v_add_u32_e32 v252, 0xffffe000, v152
	v_mov_b32_e32 v253, v3
	v_lshl_add_u64 v[252:253], v[148:149], 0, v[252:253]
	v_cvt_pk_fp8_f32 v232, v173, v177
	v_cvt_pk_fp8_f32 v233, v174, v178
	v_cvt_pk_fp8_f32 v234, v175, v179
	v_cvt_pk_fp8_f32 v235, v176, v180
	v_cvt_pk_fp8_f32 v232, v165, v166 op_sel:[0,0,1]
	v_cvt_pk_fp8_f32 v233, v167, v168 op_sel:[0,0,1]
	v_cvt_pk_fp8_f32 v234, v169, v170 op_sel:[0,0,1]
	v_cvt_pk_fp8_f32 v235, v171, v172 op_sel:[0,0,1]
	v_exp_f32_e32 v154, v154
	v_add_f32_e32 v240, v173, v177
	v_exp_f32_e32 v155, v155
	v_add_f32_e32 v240, v165, v240
	v_exp_f32_e32 v130, v130
	s_waitcnt lgkmcnt(1)
	v_mfma_scale_f32_32x32x64_f8f6f4 v[84:99], v[68:75], v[100:107], 0, v188, v188 op_sel_hi:[0,0,0]
	v_add_f32_e32 v240, v166, v240
	v_exp_f32_e32 v131, v131
	v_add_f32_e32 v240, v174, v240
	v_exp_f32_e32 v128, v128
	v_add_f32_e32 v240, v178, v240
	v_exp_f32_e32 v129, v129
	v_add_f32_e32 v240, v167, v240
	v_exp_f32_e32 v126, v126
	v_add_f32_e32 v240, v168, v240
	v_exp_f32_e32 v127, v127
	v_add_f32_e32 v240, v175, v240
	v_exp_f32_e32 v124, v124
	v_add_f32_e32 v240, v179, v240
	v_exp_f32_e32 v125, v125
	v_add_f32_e32 v240, v169, v240
	v_exp_f32_e32 v160, v160
	s_waitcnt lgkmcnt(0)
	v_mfma_scale_f32_32x32x64_f8f6f4 v[68:83], v[200:207], v[100:107], 0, v188, v188 op_sel_hi:[0,0,0]
	ds_read_b128 v[200:203], v194 offset:61440
	ds_read_b128 v[208:211], v194 offset:57344
	ds_read_b128 v[212:215], v195 offset:57344
	ds_read_b128 v[204:207], v195 offset:61440
	v_add_f32_e32 v240, v170, v240
	v_exp_f32_e32 v161, v161
	v_add_f32_e32 v240, v176, v240
	v_exp_f32_e32 v158, v158
	v_add_f32_e32 v240, v180, v240
	v_exp_f32_e32 v159, v159
	v_add_f32_e32 v240, v171, v240
	v_exp_f32_e32 v156, v156
	v_add_f32_e32 v240, v172, v240
	v_exp_f32_e32 v157, v157
	v_cvt_pk_fp8_f32 v236, v154, v155
	v_cvt_pk_fp8_f32 v237, v128, v129
	v_cvt_pk_fp8_f32 v238, v124, v125
	v_cvt_pk_fp8_f32 v239, v158, v159
	v_cvt_pk_fp8_f32 v236, v130, v131 op_sel:[0,0,1]
	v_cvt_pk_fp8_f32 v237, v126, v127 op_sel:[0,0,1]
	s_waitcnt lgkmcnt(1)
	v_mfma_scale_f32_32x32x64_f8f6f4 v[84:99], v[208:215], v[108:115], v[84:99], v188, v188 op_sel_hi:[0,0,0]
	v_cvt_pk_fp8_f32 v238, v160, v161 op_sel:[0,0,1]
	v_cvt_pk_fp8_f32 v239, v156, v157 op_sel:[0,0,1]
	v_add_f32_e32 v241, v128, v129
	v_add_f32_e32 v241, v124, v241
	v_add_f32_e32 v241, v125, v241
	v_add_f32_e32 v241, v126, v241
	v_add_f32_e32 v241, v127, v241
	v_add_f32_e32 v241, v130, v241
	v_add_f32_e32 v241, v131, v241
	v_add_f32_e32 v241, v154, v241
	v_add_f32_e32 v241, v155, v241
	v_add_f32_e32 v241, v160, v241
	v_add_f32_e32 v241, v161, v241
	v_add_f32_e32 v241, v158, v241
	v_add_f32_e32 v241, v159, v241
	v_add_f32_e32 v241, v156, v241
	s_waitcnt lgkmcnt(0)
	v_mfma_scale_f32_32x32x64_f8f6f4 v[68:83], v[200:207], v[108:115], v[68:83], v188, v188 op_sel_hi:[0,0,0]
	ds_read_b128 v[200:203], v197 offset:8192
	ds_read_b128 v[204:207], v198 offset:8192
	ds_read_b128 v[208:211], v197 offset:10240
	ds_read_b128 v[212:215], v198 offset:10240
	ds_read_b128 v[216:219], v197 offset:12288
	ds_read_b128 v[220:223], v198 offset:12288
	ds_read_b128 v[224:227], v197 offset:14336
	ds_read_b128 v[228:231], v198 offset:14336
	global_load_dwordx4 v[124:127], v[150:151], off offset:-64
	global_load_dwordx4 v[128:131], v[252:253], off
	v_add_f32_e32 v241, v157, v241
	v_add_f32_e32 v162, v240, v241
	v_mov_b32_e32 v163, v162
	s_nop 0
	s_nop 0
	v_permlane32_swap_b32_e32 v162, v163
	v_max3_f32 v246, v84, v85, v86
	v_max3_f32 v246, v246, v87, v88
	v_max3_f32 v246, v246, v89, v90
	v_max3_f32 v246, v246, v91, v92
	v_max3_f32 v246, v246, v93, v94
	v_max3_f32 v246, v246, v95, v96
	v_max3_f32 v246, v246, v97, v98
	v_max_f32_e32 v246, v246, v99
	v_max3_f32 v248, v68, v69, v70
	v_max3_f32 v248, v248, v71, v72
	v_max3_f32 v248, v248, v73, v74
	v_max3_f32 v248, v248, v75, v76
	v_max3_f32 v248, v248, v77, v78
	s_waitcnt lgkmcnt(6)
	v_mfma_scale_f32_32x32x64_f8f6f4 v[52:67], v[232:239], v[200:207], v[52:67], v188, v188 op_sel_hi:[0,0,0]
	v_max3_f32 v248, v248, v79, v80
	v_max3_f32 v248, v248, v81, v82
	v_max_f32_e32 v248, v248, v83
	v_max_f32_e32 v250, v246, v248
	v_mov_b32_e32 v251, v250
	s_nop 0
	s_nop 0
	v_permlane32_swap_b32_e32 v250, v251
	v_max_f32_e32 v250, v250, v251
	v_sub_f32_e32 v154, v250, v153
	v_max_f32_e32 v2, v153, v250
	v_sub_f32_e32 v155, v153, v2
	v_mul_f32_e32 v155, 0x3e0293ee, v155
	v_exp_f32_e32 v155, v155
	v_cmp_ge_f32_e32 vcc, s55, v154
	s_cmp_eq_u64 vcc, exec
	s_cselect_b64 s[4:5], -1, 0
	v_cndmask_b32_e64 v164, v155, 1.0, s[4:5]
	v_cmp_gt_f32_e32 vcc, 1.0, v164
	s_waitcnt lgkmcnt(4)
	v_mfma_scale_f32_32x32x64_f8f6f4 v[36:51], v[232:239], v[208:215], v[36:51], v188, v188 op_sel_hi:[0,0,0]
	v_cndmask_b32_e64 v154, v2, v153, s[4:5]
	v_mul_f32_e32 v247, 0xbe0293ee, v154
	v_fmamk_f32 v84, v84, 0x3e0293ee, v247
	v_exp_f32_e32 v165, v84
	v_fmamk_f32 v85, v85, 0x3e0293ee, v247
	v_exp_f32_e32 v169, v85
	v_fmamk_f32 v86, v86, 0x3e0293ee, v247
	v_exp_f32_e32 v2, v86
	v_fmamk_f32 v87, v87, 0x3e0293ee, v247
	v_exp_f32_e32 v155, v87
	v_fmamk_f32 v88, v88, 0x3e0293ee, v247
	v_exp_f32_e32 v166, v88
	v_fmamk_f32 v89, v89, 0x3e0293ee, v247
	v_exp_f32_e32 v170, v89
	v_fmamk_f32 v90, v90, 0x3e0293ee, v247
	v_exp_f32_e32 v156, v90
	v_fmamk_f32 v91, v91, 0x3e0293ee, v247
	s_waitcnt lgkmcnt(2)
	v_mfma_scale_f32_32x32x64_f8f6f4 v[20:35], v[232:239], v[216:223], v[20:35], v188, v188 op_sel_hi:[0,0,0]
	v_exp_f32_e32 v157, v91
	v_fmamk_f32 v92, v92, 0x3e0293ee, v247
	v_exp_f32_e32 v167, v92
	v_fmamk_f32 v93, v93, 0x3e0293ee, v247
	v_exp_f32_e32 v171, v93
	v_fmamk_f32 v94, v94, 0x3e0293ee, v247
	v_exp_f32_e32 v158, v94
	v_fmamk_f32 v95, v95, 0x3e0293ee, v247
	v_exp_f32_e32 v159, v95
	v_fmamk_f32 v96, v96, 0x3e0293ee, v247
	v_exp_f32_e32 v168, v96
	v_fmamk_f32 v97, v97, 0x3e0293ee, v247
	v_exp_f32_e32 v172, v97
	v_fmamk_f32 v98, v98, 0x3e0293ee, v247
	v_exp_f32_e32 v160, v98
	v_fmamk_f32 v99, v99, 0x3e0293ee, v247
	v_exp_f32_e32 v161, v99
	s_waitcnt lgkmcnt(0)
	v_mfma_scale_f32_32x32x64_f8f6f4 v[4:19], v[232:239], v[224:231], v[4:19], v188, v188 op_sel_hi:[0,0,0]
	v_fmamk_f32 v173, v68, 0x3e0293ee, v247
	v_fmamk_f32 v174, v69, 0x3e0293ee, v247
	v_fmamk_f32 v175, v70, 0x3e0293ee, v247
	v_fmamk_f32 v176, v71, 0x3e0293ee, v247
	v_fmamk_f32 v177, v72, 0x3e0293ee, v247
	v_fmamk_f32 v178, v73, 0x3e0293ee, v247
	v_fmamk_f32 v179, v74, 0x3e0293ee, v247
	v_fmamk_f32 v180, v75, 0x3e0293ee, v247
	v_fmamk_f32 v181, v76, 0x3e0293ee, v247
	v_fmamk_f32 v182, v77, 0x3e0293ee, v247
	v_fmamk_f32 v183, v78, 0x3e0293ee, v247
	v_fmamk_f32 v200, v79, 0x3e0293ee, v247
	v_fmamk_f32 v201, v80, 0x3e0293ee, v247
	v_fmamk_f32 v208, v81, 0x3e0293ee, v247
	v_fmamk_f32 v209, v82, 0x3e0293ee, v247
	v_fmamk_f32 v153, v83, 0x3e0293ee, v247
	s_cbranch_vccz .Lring_noresc_a1
	s_nop 15
	s_nop 7
	s_and_saveexec_b64 s[8:9], s[6:7]
	ds_write_b32 v184, v164 offset:128
	s_or_b64 exec, exec, s[8:9]
	s_waitcnt lgkmcnt(0)
	v_add_u32_e32 v228, v135, v185
	ds_read_b128 v[224:227], v228 offset:224
	ds_read_b128 v[220:223], v228 offset:192
	ds_read_b128 v[216:219], v228 offset:160
	ds_read_b128 v[212:215], v228 offset:128
	s_waitcnt lgkmcnt(0)
	v_pk_mul_f32 v[52:53], v[52:53], v[212:213]
	v_pk_mul_f32 v[54:55], v[54:55], v[214:215]
	v_pk_mul_f32 v[56:57], v[56:57], v[216:217]
	v_pk_mul_f32 v[58:59], v[58:59], v[218:219]
	v_pk_mul_f32 v[60:61], v[60:61], v[220:221]
	v_pk_mul_f32 v[62:63], v[62:63], v[222:223]
	v_pk_mul_f32 v[64:65], v[64:65], v[224:225]
	v_pk_mul_f32 v[66:67], v[66:67], v[226:227]
	v_pk_mul_f32 v[36:37], v[36:37], v[212:213]
	v_pk_mul_f32 v[38:39], v[38:39], v[214:215]
	v_pk_mul_f32 v[40:41], v[40:41], v[216:217]
	v_pk_mul_f32 v[42:43], v[42:43], v[218:219]
	v_pk_mul_f32 v[44:45], v[44:45], v[220:221]
	v_pk_mul_f32 v[46:47], v[46:47], v[222:223]
	v_pk_mul_f32 v[48:49], v[48:49], v[224:225]
	v_pk_mul_f32 v[50:51], v[50:51], v[226:227]
	v_pk_mul_f32 v[20:21], v[20:21], v[212:213]
	v_pk_mul_f32 v[22:23], v[22:23], v[214:215]
	v_pk_mul_f32 v[24:25], v[24:25], v[216:217]
	v_pk_mul_f32 v[26:27], v[26:27], v[218:219]
	v_pk_mul_f32 v[28:29], v[28:29], v[220:221]
	v_pk_mul_f32 v[30:31], v[30:31], v[222:223]
	v_pk_mul_f32 v[32:33], v[32:33], v[224:225]
	v_pk_mul_f32 v[34:35], v[34:35], v[226:227]
	v_pk_mul_f32 v[4:5], v[4:5], v[212:213]
	v_pk_mul_f32 v[6:7], v[6:7], v[214:215]
	v_pk_mul_f32 v[8:9], v[8:9], v[216:217]
	v_pk_mul_f32 v[10:11], v[10:11], v[218:219]
	v_pk_mul_f32 v[12:13], v[12:13], v[220:221]
	v_pk_mul_f32 v[14:15], v[14:15], v[222:223]
	v_pk_mul_f32 v[16:17], v[16:17], v[224:225]
	v_pk_mul_f32 v[18:19], v[18:19], v[226:227]
.Lring_noresc_a1:
	s_waitcnt lgkmcnt(0)
	s_barrier
	s_waitcnt vmcnt(0)
	v_mov_b32_e32 v254, v124
	v_mov_b32_e32 v255, v126
	ds_write_b64 v189, v[254:255] offset:16384
	v_mov_b32_e32 v244, v125
	v_mov_b32_e32 v245, v127
	ds_write_b64 v190, v[244:245] offset:16384
	ds_write_b128 v191, v[128:131] offset:49152
	s_cmp_gt_u32 s15, 60
	s_cselect_b64 s[8:9], -1, 0
	s_and_b64 vcc, exec, s[8:9]
	s_cbranch_vccnz .Lring_noload_b1
	v_mov_b32_e32 v252, v152
	v_mov_b32_e32 v253, v3
	v_lshl_add_u64 v[120:121], v[148:149], 0, v[252:253]
	global_load_dwordx4 v[116:119], v[150:151], off
	s_nop 0
	global_load_dwordx4 v[120:123], v[120:121], off
.Lring_noload_b1:
	ds_read_b128 v[210:213], v192 offset:36864
	ds_read_b128 v[68:71], v192 offset:32768
	ds_read_b128 v[72:75], v193 offset:32768
	ds_read_b128 v[214:217], v193 offset:36864
	v_cvt_pk_fp8_f32 v232, v165, v169
	v_cvt_pk_fp8_f32 v233, v166, v170
	v_cvt_pk_fp8_f32 v234, v167, v171
	v_cvt_pk_fp8_f32 v235, v168, v172
	v_cvt_pk_fp8_f32 v232, v2, v155 op_sel:[0,0,1]
	v_cvt_pk_fp8_f32 v233, v156, v157 op_sel:[0,0,1]
	v_cvt_pk_fp8_f32 v234, v158, v159 op_sel:[0,0,1]
	v_cvt_pk_fp8_f32 v235, v160, v161 op_sel:[0,0,1]
	v_exp_f32_e32 v173, v173
	v_add_f32_e32 v240, v165, v169
	v_exp_f32_e32 v174, v174
	v_add_f32_e32 v240, v2, v240
	v_exp_f32_e32 v175, v175
	v_add_f32_e32 v240, v155, v240
	v_exp_f32_e32 v176, v176
	v_add_f32_e32 v240, v166, v240
	s_waitcnt lgkmcnt(1)
	v_mfma_scale_f32_32x32x64_f8f6f4 v[84:99], v[68:75], v[100:107], 0, v188, v188 op_sel_hi:[0,0,0]
	v_exp_f32_e32 v177, v177
	v_add_f32_e32 v240, v170, v240
	v_exp_f32_e32 v178, v178
	v_add_f32_e32 v240, v156, v240
	v_exp_f32_e32 v179, v179
	v_add_f32_e32 v240, v157, v240
	v_exp_f32_e32 v180, v180
	v_add_f32_e32 v240, v167, v240
	v_exp_f32_e32 v181, v181
	v_add_f32_e32 v240, v171, v240
	v_exp_f32_e32 v182, v182
	v_add_f32_e32 v240, v158, v240
	v_exp_f32_e32 v183, v183
	v_add_f32_e32 v240, v159, v240
	v_exp_f32_e32 v200, v200
	v_add_f32_e32 v240, v168, v240
	s_waitcnt lgkmcnt(0)
	v_mfma_scale_f32_32x32x64_f8f6f4 v[68:83], v[210:217], v[100:107], 0, v188, v188 op_sel_hi:[0,0,0]
	ds_read_b128 v[210:213], v194 offset:36864
	ds_read_b128 v[218:221], v194 offset:32768
	ds_read_b128 v[222:225], v195 offset:32768
	ds_read_b128 v[214:217], v195 offset:36864
	v_exp_f32_e32 v201, v201
	v_add_f32_e32 v240, v172, v240
	v_exp_f32_e32 v208, v208
	v_add_f32_e32 v240, v160, v240
	v_exp_f32_e32 v209, v209
	v_add_f32_e32 v240, v161, v240
	v_exp_f32_e32 v153, v153
	v_cvt_pk_fp8_f32 v236, v173, v174
	v_cvt_pk_fp8_f32 v237, v177, v178
	v_cvt_pk_fp8_f32 v238, v181, v182
	v_cvt_pk_fp8_f32 v239, v201, v208
	v_cvt_pk_fp8_f32 v236, v175, v176 op_sel:[0,0,1]
	v_cvt_pk_fp8_f32 v237, v179, v180 op_sel:[0,0,1]
	v_cvt_pk_fp8_f32 v238, v183, v200 op_sel:[0,0,1]
	v_cvt_pk_fp8_f32 v239, v209, v153 op_sel:[0,0,1]
	v_add_f32_e32 v241, v173, v200
	s_waitcnt lgkmcnt(1)
	v_mfma_scale_f32_32x32x64_f8f6f4 v[84:99], v[218:225], v[108:115], v[84:99], v188, v188 op_sel_hi:[0,0,0]
	v_add_f32_e32 v241, v201, v241
	v_add_f32_e32 v241, v174, v241
	v_add_f32_e32 v241, v175, v241
	v_add_f32_e32 v241, v176, v241
	v_add_f32_e32 v241, v177, v241
	v_add_f32_e32 v241, v178, v241
	v_add_f32_e32 v241, v179, v241
	v_add_f32_e32 v241, v180, v241
	v_add_f32_e32 v241, v181, v241
	v_add_f32_e32 v241, v182, v241
	v_add_f32_e32 v241, v183, v241
	v_add_f32_e32 v241, v208, v241
	v_add_f32_e32 v241, v209, v241
	v_add_f32_e32 v241, v153, v241
	v_add_f32_e32 v181, v240, v241
	v_mov_b32_e32 v182, v181
	s_nop 0
	s_nop 0
	v_permlane32_swap_b32_e32 v181, v182
	s_waitcnt lgkmcnt(0)
	v_mfma_scale_f32_32x32x64_f8f6f4 v[68:83], v[210:217], v[108:115], v[68:83], v188, v188 op_sel_hi:[0,0,0]
	ds_read_b128 v[200:203], v197 offset:24576
	ds_read_b128 v[204:207], v198 offset:24576
	ds_read_b128 v[208:211], v197 offset:26624
	ds_read_b128 v[212:215], v198 offset:26624
	ds_read_b128 v[216:219], v197 offset:28672
	ds_read_b128 v[220:223], v198 offset:28672
	ds_read_b128 v[224:227], v197 offset:30720
	ds_read_b128 v[228:231], v198 offset:30720
	v_max3_f32 v246, v84, v85, v86
	v_max3_f32 v246, v246, v87, v88
	v_max3_f32 v246, v246, v89, v90
	v_max3_f32 v246, v246, v91, v92
	v_max3_f32 v246, v246, v93, v94
	v_max3_f32 v246, v246, v95, v96
	v_max3_f32 v246, v246, v97, v98
	v_max_f32_e32 v246, v246, v99
	s_nop 3
	v_max3_f32 v248, v68, v69, v70
	v_max3_f32 v248, v248, v71, v72
	v_max3_f32 v248, v248, v73, v74
	v_max3_f32 v248, v248, v75, v76
	v_max3_f32 v248, v248, v77, v78
	v_max3_f32 v248, v248, v79, v80
	v_max3_f32 v248, v248, v81, v82
	v_max_f32_e32 v248, v248, v83
	v_max_f32_e32 v250, v246, v248
	s_waitcnt lgkmcnt(6)
	v_mfma_scale_f32_32x32x64_f8f6f4 v[52:67], v[232:239], v[200:207], v[52:67], v188, v188 op_sel_hi:[0,0,0]
	v_mov_b32_e32 v251, v250
	s_nop 1
	v_permlane32_swap_b32_e32 v250, v251
	v_max_f32_e32 v250, v250, v251
	v_sub_f32_e32 v155, v250, v154
	v_max_f32_e32 v153, v154, v250
	v_sub_f32_e32 v2, v154, v153
	v_mul_f32_e32 v2, 0x3e0293ee, v2
	v_exp_f32_e32 v2, v2
	v_cmp_ge_f32_e32 vcc, s55, v155
	s_cmp_eq_u64 vcc, exec
	s_cselect_b64 s[4:5], -1, 0
	v_cndmask_b32_e64 v2, v2, 1.0, s[4:5]
	v_cmp_gt_f32_e32 vcc, 1.0, v2
	v_cndmask_b32_e64 v153, v153, v154, s[4:5]
	v_mul_f32_e32 v247, 0xbe0293ee, v153
	v_fmamk_f32 v84, v84, 0x3e0293ee, v247
	v_exp_f32_e32 v173, v84
	s_waitcnt lgkmcnt(4)
	v_mfma_scale_f32_32x32x64_f8f6f4 v[36:51], v[232:239], v[208:215], v[36:51], v188, v188 op_sel_hi:[0,0,0]
	v_fmamk_f32 v85, v85, 0x3e0293ee, v247
	v_exp_f32_e32 v177, v85
	v_fmamk_f32 v86, v86, 0x3e0293ee, v247
	v_exp_f32_e32 v165, v86
	v_fmamk_f32 v87, v87, 0x3e0293ee, v247
	v_exp_f32_e32 v166, v87
	v_fmamk_f32 v88, v88, 0x3e0293ee, v247
	v_exp_f32_e32 v174, v88
	v_fmamk_f32 v89, v89, 0x3e0293ee, v247
	v_exp_f32_e32 v178, v89
	v_fmamk_f32 v90, v90, 0x3e0293ee, v247
	v_exp_f32_e32 v167, v90
	v_fmamk_f32 v91, v91, 0x3e0293ee, v247
	v_exp_f32_e32 v168, v91
	v_fmamk_f32 v92, v92, 0x3e0293ee, v247
	v_exp_f32_e32 v175, v92
	v_fmamk_f32 v93, v93, 0x3e0293ee, v247
	s_waitcnt lgkmcnt(2)
	v_mfma_scale_f32_32x32x64_f8f6f4 v[20:35], v[232:239], v[216:223], v[20:35], v188, v188 op_sel_hi:[0,0,0]
	v_exp_f32_e32 v179, v93
	v_fmamk_f32 v94, v94, 0x3e0293ee, v247
	v_exp_f32_e32 v169, v94
	v_fmamk_f32 v95, v95, 0x3e0293ee, v247
	v_exp_f32_e32 v170, v95
	v_fmamk_f32 v96, v96, 0x3e0293ee, v247
	v_exp_f32_e32 v176, v96
	v_fmamk_f32 v97, v97, 0x3e0293ee, v247
	v_exp_f32_e32 v180, v97
	v_fmamk_f32 v98, v98, 0x3e0293ee, v247
	v_exp_f32_e32 v171, v98
	v_fmamk_f32 v99, v99, 0x3e0293ee, v247
	v_exp_f32_e32 v172, v99
	v_fmamk_f32 v154, v68, 0x3e0293ee, v247
	v_fmamk_f32 v155, v69, 0x3e0293ee, v247
	v_fmamk_f32 v130, v70, 0x3e0293ee, v247
	v_fmamk_f32 v131, v71, 0x3e0293ee, v247
	s_waitcnt lgkmcnt(0)
	v_mfma_scale_f32_32x32x64_f8f6f4 v[4:19], v[232:239], v[224:231], v[4:19], v188, v188 op_sel_hi:[0,0,0]
	v_fmamk_f32 v128, v72, 0x3e0293ee, v247
	v_fmamk_f32 v129, v73, 0x3e0293ee, v247
	v_fmamk_f32 v126, v74, 0x3e0293ee, v247
	v_fmamk_f32 v127, v75, 0x3e0293ee, v247
	v_fmamk_f32 v124, v76, 0x3e0293ee, v247
	v_fmamk_f32 v125, v77, 0x3e0293ee, v247
	v_fmamk_f32 v160, v78, 0x3e0293ee, v247
	v_fmamk_f32 v161, v79, 0x3e0293ee, v247
	v_fmamk_f32 v158, v80, 0x3e0293ee, v247
	v_fmamk_f32 v159, v81, 0x3e0293ee, v247
	v_fmamk_f32 v156, v82, 0x3e0293ee, v247
	v_fmamk_f32 v157, v83, 0x3e0293ee, v247
	v_add_f32_e32 v249, v162, v163
	v_fmac_f32_e32 v249, v147, v145
	v_add_f32_e32 v145, v181, v182
	v_fmac_f32_e32 v145, v249, v164
	s_cbranch_vccz .Lring_noresc_b1
	s_nop 15
	s_nop 7
	s_and_saveexec_b64 s[10:11], s[6:7]
	ds_write_b32 v184, v2 offset:128
	s_or_b64 exec, exec, s[10:11]
	s_waitcnt lgkmcnt(0)
	v_add_u32_e32 v228, v135, v185
	ds_read_b128 v[224:227], v228 offset:224
	ds_read_b128 v[220:223], v228 offset:192
	ds_read_b128 v[216:219], v228 offset:160
	ds_read_b128 v[212:215], v228 offset:128
	s_waitcnt lgkmcnt(0)
	v_pk_mul_f32 v[52:53], v[52:53], v[212:213]
	v_pk_mul_f32 v[54:55], v[54:55], v[214:215]
	v_pk_mul_f32 v[56:57], v[56:57], v[216:217]
	v_pk_mul_f32 v[58:59], v[58:59], v[218:219]
	v_pk_mul_f32 v[60:61], v[60:61], v[220:221]
	v_pk_mul_f32 v[62:63], v[62:63], v[222:223]
	v_pk_mul_f32 v[64:65], v[64:65], v[224:225]
	v_pk_mul_f32 v[66:67], v[66:67], v[226:227]
	v_pk_mul_f32 v[36:37], v[36:37], v[212:213]
	v_pk_mul_f32 v[38:39], v[38:39], v[214:215]
	v_pk_mul_f32 v[40:41], v[40:41], v[216:217]
	v_pk_mul_f32 v[42:43], v[42:43], v[218:219]
	v_pk_mul_f32 v[44:45], v[44:45], v[220:221]
	v_pk_mul_f32 v[46:47], v[46:47], v[222:223]
	v_pk_mul_f32 v[48:49], v[48:49], v[224:225]
	v_pk_mul_f32 v[50:51], v[50:51], v[226:227]
	v_pk_mul_f32 v[20:21], v[20:21], v[212:213]
	v_pk_mul_f32 v[22:23], v[22:23], v[214:215]
	v_pk_mul_f32 v[24:25], v[24:25], v[216:217]
	v_pk_mul_f32 v[26:27], v[26:27], v[218:219]
	v_pk_mul_f32 v[28:29], v[28:29], v[220:221]
	v_pk_mul_f32 v[30:31], v[30:31], v[222:223]
	v_pk_mul_f32 v[32:33], v[32:33], v[224:225]
	v_pk_mul_f32 v[34:35], v[34:35], v[226:227]
	v_pk_mul_f32 v[4:5], v[4:5], v[212:213]
	v_pk_mul_f32 v[6:7], v[6:7], v[214:215]
	v_pk_mul_f32 v[8:9], v[8:9], v[216:217]
	v_pk_mul_f32 v[10:11], v[10:11], v[218:219]
	v_pk_mul_f32 v[12:13], v[12:13], v[220:221]
	v_pk_mul_f32 v[14:15], v[14:15], v[222:223]
	v_pk_mul_f32 v[16:17], v[16:17], v[224:225]
	v_pk_mul_f32 v[18:19], v[18:19], v[226:227]
.Lring_noresc_b1:
	s_add_i32 s15, s15, 2
	v_lshl_add_u64 v[150:151], v[150:151], 0, s[28:29]
	v_add_u32_e32 v152, 0x4000, v152
	s_and_b64 vcc, exec, s[8:9]
	s_waitcnt lgkmcnt(0)
	s_barrier
	s_cbranch_vccnz .LBB0_421
	v_mov_b32_e32 v147, v2
	s_branch .LBB0_409
.LBB0_421:
	ds_read_b128 v[116:119], v192 offset:61440
	ds_read_b128 v[68:71], v192 offset:57344
	ds_read_b128 v[72:75], v193 offset:57344
	ds_read_b128 v[120:123], v193 offset:61440
	s_waitcnt lgkmcnt(1)
	v_mfma_scale_f32_32x32x64_f8f6f4 v[84:99], v[68:75], v[100:107], 0, v188, v188 op_sel_hi:[0,0,0]
	s_waitcnt lgkmcnt(0)
	v_mfma_scale_f32_32x32x64_f8f6f4 v[68:83], v[116:123], v[100:107], 0, v188, v188 op_sel_hi:[0,0,0]
	ds_read_b128 v[100:103], v194 offset:61440
	ds_read_b128 v[116:119], v194 offset:57344
	ds_read_b128 v[120:123], v195 offset:57344
	ds_read_b128 v[104:107], v195 offset:61440
	s_waitcnt lgkmcnt(1)
	v_mfma_scale_f32_32x32x64_f8f6f4 v[84:99], v[116:123], v[108:115], v[84:99], v188, v188 op_sel_hi:[0,0,0]
	s_waitcnt lgkmcnt(0)
	v_mfma_scale_f32_32x32x64_f8f6f4 v[68:83], v[100:107], v[108:115], v[68:83], v188, v188 op_sel_hi:[0,0,0]
	v_add_f32_e32 v100, 0, v173
	v_add_f32_e32 v100, v177, v100
	v_add_f32_e32 v100, v165, v100
	v_add_f32_e32 v100, v166, v100
	v_add_f32_e32 v100, v174, v100
	v_add_f32_e32 v100, v178, v100
	v_add_f32_e32 v100, v167, v100
	v_add_f32_e32 v100, v168, v100
	v_add_f32_e32 v100, v175, v100
	v_add_f32_e32 v100, v179, v100
	v_add_f32_e32 v100, v169, v100
	v_add_f32_e32 v100, v170, v100
	v_exp_f32_e32 v101, v154
	v_add_f32_e32 v100, v176, v100
	v_exp_f32_e32 v107, v155
	v_add_f32_e32 v100, v180, v100
	v_exp_f32_e32 v110, v130
	v_add_f32_e32 v100, v171, v100
	v_exp_f32_e32 v111, v131
	v_add_f32_e32 v100, v172, v100
	v_exp_f32_e32 v108, v128
	v_add_f32_e32 v100, v101, v100
	v_exp_f32_e32 v109, v129
	v_add_f32_e32 v100, v107, v100
	v_exp_f32_e32 v112, v126
	v_add_f32_e32 v100, v110, v100
	v_exp_f32_e32 v113, v127
	v_add_f32_e32 v100, v111, v100
	v_exp_f32_e32 v114, v124
	v_add_f32_e32 v100, v108, v100
	v_exp_f32_e32 v115, v125
	v_add_f32_e32 v100, v109, v100
	v_exp_f32_e32 v116, v160
	v_add_f32_e32 v100, v112, v100
	v_exp_f32_e32 v117, v161
	v_add_f32_e32 v100, v113, v100
	v_exp_f32_e32 v118, v158
	v_add_f32_e32 v100, v114, v100
	v_exp_f32_e32 v119, v159
	v_add_f32_e32 v100, v115, v100
	v_mov_b32_e32 v102, v3
	v_mov_b32_e32 v103, v3
	v_exp_f32_e32 v120, v156
	v_add_f32_e32 v100, v116, v100
	v_cvt_pk_fp8_f32 v102, v173, v177
	v_cvt_pk_fp8_f32 v103, v174, v178
	v_exp_f32_e32 v121, v157
	v_add_f32_e32 v100, v117, v100
	v_mov_b32_e32 v106, v3
	v_add_f32_e32 v100, v118, v100
	v_cvt_pk_fp8_f32 v106, v101, v107
	v_mov_b32_e32 v107, v3
	v_add_f32_e32 v100, v119, v100
	v_mov_b32_e32 v104, v3
	v_mov_b32_e32 v105, v3
	v_cvt_pk_fp8_f32 v107, v108, v109
	v_mov_b32_e32 v108, v3
	v_mov_b32_e32 v109, v3
	v_add_f32_e32 v100, v120, v100
	v_cvt_pk_fp8_f32 v104, v175, v179
	v_cvt_pk_fp8_f32 v105, v176, v180
	v_cvt_pk_fp8_f32 v102, v165, v166 op_sel:[0,0,1]
	v_cvt_pk_fp8_f32 v103, v167, v168 op_sel:[0,0,1]
	v_cvt_pk_fp8_f32 v108, v114, v115
	v_cvt_pk_fp8_f32 v109, v118, v119
	v_add_f32_e32 v100, v121, v100
	v_mov_b32_e32 v101, v100
	s_nop 1
	v_permlane32_swap_b32_e32 v100, v101
	s_nop 15
	s_nop 15
	v_cvt_pk_fp8_f32 v104, v169, v170 op_sel:[0,0,1]
	v_cvt_pk_fp8_f32 v105, v171, v172 op_sel:[0,0,1]
	v_cvt_pk_fp8_f32 v106, v110, v111 op_sel:[0,0,1]
	v_cvt_pk_fp8_f32 v107, v112, v113 op_sel:[0,0,1]
	v_cvt_pk_fp8_f32 v108, v116, v117 op_sel:[0,0,1]
	v_cvt_pk_fp8_f32 v109, v120, v121 op_sel:[0,0,1]
	ds_read_b128 v[110:113], v197 offset:8192
	ds_read_b128 v[118:121], v197 offset:10240
	ds_read_b128 v[114:117], v198 offset:8192
	ds_read_b128 v[122:125], v198 offset:10240
	ds_read_b128 v[154:157], v197 offset:12288
	ds_read_b128 v[162:165], v197 offset:14336
	ds_read_b128 v[158:161], v198 offset:12288
	ds_read_b128 v[166:169], v198 offset:14336
	s_waitcnt lgkmcnt(5)
	v_mfma_scale_f32_32x32x64_f8f6f4 v[52:67], v[102:109], v[110:117], v[52:67], v188, v188 op_sel_hi:[0,0,0]
	s_waitcnt lgkmcnt(4)
	v_mfma_scale_f32_32x32x64_f8f6f4 v[36:51], v[102:109], v[118:125], v[36:51], v188, v188 op_sel_hi:[0,0,0]
	s_waitcnt lgkmcnt(1)
	v_mfma_scale_f32_32x32x64_f8f6f4 v[20:35], v[102:109], v[154:161], v[20:35], v188, v188 op_sel_hi:[0,0,0]
	s_waitcnt lgkmcnt(0)
	v_mfma_scale_f32_32x32x64_f8f6f4 v[4:19], v[102:109], v[162:169], v[4:19], v188, v188 op_sel_hi:[0,0,0]
	v_max_f32_e32 v102, v85, v85
	v_max_f32_e32 v103, v84, v84
	v_max_f32_e32 v102, v103, v102
	v_max3_f32 v102, v102, v86, v87
	v_max3_f32 v102, v102, v88, v89
	v_max3_f32 v102, v102, v90, v91
	v_max3_f32 v102, v102, v92, v93
	v_max3_f32 v102, v102, v94, v95
	v_max3_f32 v102, v102, v96, v97
	v_max3_f32 v102, v102, v98, v99
	v_max3_f32 v102, v102, v68, v69
	v_max3_f32 v102, v102, v70, v71
	v_max3_f32 v102, v102, v72, v73
	v_max3_f32 v102, v102, v74, v75
	v_max3_f32 v102, v102, v76, v77
	v_max3_f32 v102, v102, v78, v79
	v_max3_f32 v102, v102, v80, v81
	v_max3_f32 v102, v102, v82, v83
	v_mov_b32_e32 v103, v102
	s_nop 1
	v_permlane32_swap_b32_e32 v102, v103
	v_max_f32_e32 v103, v103, v103
	v_max_f32_e32 v102, v102, v102
	v_max_f32_e32 v102, v102, v103
	v_max_f32_e32 v103, v153, v153
	v_max_f32_e32 v103, v103, v102
	v_sub_f32_e32 v104, v102, v153
	v_sub_f32_e32 v102, v153, v103
	v_mul_f32_e32 v102, 0x3e0293ee, v102
	v_exp_f32_e32 v102, v102
	v_cmp_ge_f32_e32 vcc, s55, v104
	s_cmp_eq_u64 vcc, exec
	s_cselect_b64 s[4:5], -1, 0
	v_cndmask_b32_e64 v102, v102, 1.0, s[4:5]
	v_cmp_gt_f32_e32 vcc, 1.0, v102
	s_nop 15
	s_nop 15
	s_barrier
	s_cbranch_vccz .LBB0_425
	s_and_saveexec_b64 s[8:9], s[6:7]
	ds_write_b32 v184, v102 offset:128
	s_or_b64 exec, exec, s[8:9]
	s_waitcnt lgkmcnt(0)
	v_add_u32_e32 v116, v135, v185
	ds_read_b128 v[104:107], v116 offset:224
	ds_read_b128 v[108:111], v116 offset:192
	ds_read_b128 v[112:115], v116 offset:160
	ds_read_b128 v[116:119], v116 offset:128
	s_waitcnt lgkmcnt(3)
	v_pk_mul_f32 v[64:65], v[64:65], v[104:105]
	s_waitcnt lgkmcnt(2)
	v_pk_mul_f32 v[60:61], v[60:61], v[108:109]
	s_waitcnt lgkmcnt(1)
	v_pk_mul_f32 v[56:57], v[56:57], v[112:113]
	v_pk_mul_f32 v[66:67], v[66:67], v[106:107]
	v_pk_mul_f32 v[62:63], v[62:63], v[110:111]
	v_pk_mul_f32 v[58:59], v[58:59], v[114:115]
	s_waitcnt lgkmcnt(0)
	v_pk_mul_f32 v[54:55], v[54:55], v[118:119]
	v_pk_mul_f32 v[52:53], v[52:53], v[116:117]
	v_pk_mul_f32 v[48:49], v[48:49], v[104:105]
	v_pk_mul_f32 v[44:45], v[44:45], v[108:109]
	v_pk_mul_f32 v[40:41], v[40:41], v[112:113]
	v_pk_mul_f32 v[50:51], v[50:51], v[106:107]
	v_pk_mul_f32 v[46:47], v[46:47], v[110:111]
	v_pk_mul_f32 v[42:43], v[42:43], v[114:115]
	v_pk_mul_f32 v[38:39], v[38:39], v[118:119]
	v_pk_mul_f32 v[36:37], v[36:37], v[116:117]
	v_pk_mul_f32 v[32:33], v[32:33], v[104:105]
	v_pk_mul_f32 v[28:29], v[28:29], v[108:109]
	v_pk_mul_f32 v[24:25], v[24:25], v[112:113]
	v_pk_mul_f32 v[34:35], v[34:35], v[106:107]
	v_pk_mul_f32 v[30:31], v[30:31], v[110:111]
	v_pk_mul_f32 v[26:27], v[26:27], v[114:115]
	v_pk_mul_f32 v[22:23], v[22:23], v[118:119]
	v_pk_mul_f32 v[20:21], v[20:21], v[116:117]
	v_pk_mul_f32 v[16:17], v[16:17], v[104:105]
	v_pk_mul_f32 v[12:13], v[12:13], v[108:109]
	v_pk_mul_f32 v[8:9], v[8:9], v[112:113]
	v_pk_mul_f32 v[18:19], v[18:19], v[106:107]
	v_pk_mul_f32 v[14:15], v[14:15], v[110:111]
	v_pk_mul_f32 v[10:11], v[10:11], v[114:115]
	v_pk_mul_f32 v[6:7], v[6:7], v[118:119]
	v_pk_mul_f32 v[4:5], v[4:5], v[116:117]
.LBB0_425:
	v_cndmask_b32_e64 v103, v103, v153, s[4:5]
	v_mul_f32_e32 v103, 0xbe0293ee, v103
	v_fmamk_f32 v84, v84, 0x3e0293ee, v103
	v_fmamk_f32 v85, v85, 0x3e0293ee, v103
	v_fmamk_f32 v112, v96, 0x3e0293ee, v103
	v_fmamk_f32 v96, v77, 0x3e0293ee, v103
	v_exp_f32_e32 v77, v84
	v_fmamk_f32 v86, v86, 0x3e0293ee, v103
	v_exp_f32_e32 v84, v85
	v_fmamk_f32 v87, v87, 0x3e0293ee, v103
	v_fmamk_f32 v104, v88, 0x3e0293ee, v103
	v_fmamk_f32 v88, v69, 0x3e0293ee, v103
	v_exp_f32_e32 v69, v86
	v_fmamk_f32 v105, v89, 0x3e0293ee, v103
	v_fmamk_f32 v68, v68, 0x3e0293ee, v103
	v_fmamk_f32 v89, v70, 0x3e0293ee, v103
	v_exp_f32_e32 v70, v87
	v_fmamk_f32 v113, v97, 0x3e0293ee, v103
	v_fmamk_f32 v97, v78, 0x3e0293ee, v103
	v_exp_f32_e32 v78, v104
	v_exp_f32_e32 v104, v68
	v_add_f32_e32 v68, 0, v77
	v_fmamk_f32 v106, v90, 0x3e0293ee, v103
	v_exp_f32_e32 v85, v105
	v_add_f32_e32 v68, v84, v68
	v_fmamk_f32 v107, v91, 0x3e0293ee, v103
	v_fmamk_f32 v90, v71, 0x3e0293ee, v103
	v_exp_f32_e32 v71, v106
	v_add_f32_e32 v68, v69, v68
	v_fmamk_f32 v108, v92, 0x3e0293ee, v103
	v_fmamk_f32 v91, v72, 0x3e0293ee, v103
	v_exp_f32_e32 v72, v107
	v_add_f32_e32 v68, v70, v68
	v_fmamk_f32 v109, v93, 0x3e0293ee, v103
	v_fmamk_f32 v114, v98, 0x3e0293ee, v103
	v_fmamk_f32 v98, v79, 0x3e0293ee, v103
	v_exp_f32_e32 v79, v108
	v_add_f32_e32 v68, v78, v68
	v_fmamk_f32 v110, v94, 0x3e0293ee, v103
	v_exp_f32_e32 v86, v109
	v_add_f32_e32 v68, v85, v68
	v_fmamk_f32 v111, v95, 0x3e0293ee, v103
	v_fmamk_f32 v92, v73, 0x3e0293ee, v103
	v_exp_f32_e32 v73, v110
	v_add_f32_e32 v68, v71, v68
	v_fmamk_f32 v93, v74, 0x3e0293ee, v103
	v_exp_f32_e32 v74, v111
	v_add_f32_e32 v68, v72, v68
	v_fmamk_f32 v115, v99, 0x3e0293ee, v103
	v_fmamk_f32 v99, v80, 0x3e0293ee, v103
	v_exp_f32_e32 v80, v112
	v_add_f32_e32 v68, v79, v68
	v_exp_f32_e32 v87, v113
	v_add_f32_e32 v68, v86, v68
	v_fmamk_f32 v94, v75, 0x3e0293ee, v103
	v_exp_f32_e32 v75, v114
	v_add_f32_e32 v68, v73, v68
	v_fmamk_f32 v95, v76, 0x3e0293ee, v103
	v_exp_f32_e32 v76, v115
	v_add_f32_e32 v68, v74, v68
	v_add_f32_e32 v68, v80, v68
	v_exp_f32_e32 v88, v88
	v_add_f32_e32 v68, v87, v68
	v_exp_f32_e32 v105, v89
	v_add_f32_e32 v68, v75, v68
	v_exp_f32_e32 v90, v90
	v_add_f32_e32 v68, v76, v68
	v_exp_f32_e32 v89, v91
	v_add_f32_e32 v68, v104, v68
	v_exp_f32_e32 v91, v92
	v_add_f32_e32 v68, v88, v68
	v_exp_f32_e32 v92, v93
	v_add_f32_e32 v68, v105, v68
	v_exp_f32_e32 v93, v94
	v_add_f32_e32 v68, v90, v68
	v_exp_f32_e32 v94, v95
	v_add_f32_e32 v68, v89, v68
	v_exp_f32_e32 v95, v96
	v_add_f32_e32 v68, v91, v68
	v_exp_f32_e32 v96, v97
	v_add_f32_e32 v68, v92, v68
	v_exp_f32_e32 v97, v98
	v_add_f32_e32 v68, v93, v68
	v_fmamk_f32 v81, v81, 0x3e0293ee, v103
	v_exp_f32_e32 v98, v99
	v_add_f32_e32 v68, v94, v68
	v_fmamk_f32 v82, v82, 0x3e0293ee, v103
	v_exp_f32_e32 v81, v81
	v_add_f32_e32 v68, v95, v68
	v_fmac_f32_e32 v103, 0x3e0293ee, v83
	v_exp_f32_e32 v99, v82
	v_add_f32_e32 v68, v96, v68
	v_mov_b32_e32 v82, v3
	v_mov_b32_e32 v83, v3
	v_exp_f32_e32 v103, v103
	v_add_f32_e32 v68, v97, v68
	v_cvt_pk_fp8_f32 v82, v77, v84
	v_cvt_pk_fp8_f32 v83, v78, v85
	v_mov_b32_e32 v84, v3
	v_mov_b32_e32 v85, v3
	v_add_f32_e32 v68, v98, v68
	v_cvt_pk_fp8_f32 v84, v79, v86
	v_cvt_pk_fp8_f32 v85, v80, v87
	v_mov_b32_e32 v86, v3
	v_mov_b32_e32 v87, v3
	v_add_f32_e32 v68, v81, v68
	v_cvt_pk_fp8_f32 v86, v104, v88
	v_cvt_pk_fp8_f32 v87, v89, v91
	v_mov_b32_e32 v88, v3
	v_mov_b32_e32 v89, v3
	v_add_f32_e32 v68, v99, v68
	v_cvt_pk_fp8_f32 v88, v94, v95
	v_cvt_pk_fp8_f32 v89, v98, v81
	v_add_f32_e32 v68, v103, v68
	v_cvt_pk_fp8_f32 v82, v69, v70 op_sel:[0,0,1]
	v_mov_b32_e32 v69, v68
	s_nop 1
	v_permlane32_swap_b32_e32 v68, v69
	v_cvt_pk_fp8_f32 v83, v71, v72 op_sel:[0,0,1]
	v_cvt_pk_fp8_f32 v84, v73, v74 op_sel:[0,0,1]
	v_cvt_pk_fp8_f32 v85, v75, v76 op_sel:[0,0,1]
	v_cvt_pk_fp8_f32 v86, v105, v90 op_sel:[0,0,1]
	v_cvt_pk_fp8_f32 v87, v92, v93 op_sel:[0,0,1]
	v_cvt_pk_fp8_f32 v88, v96, v97 op_sel:[0,0,1]
	v_cvt_pk_fp8_f32 v89, v99, v103 op_sel:[0,0,1]
	ds_read_b128 v[70:73], v197 offset:24576
	ds_read_b128 v[90:93], v197 offset:26624
	ds_read_b128 v[74:77], v198 offset:24576
	ds_read_b128 v[94:97], v198 offset:26624
	ds_read_b128 v[104:107], v197 offset:28672
	ds_read_b128 v[112:115], v197 offset:30720
	ds_read_b128 v[108:111], v198 offset:28672
	ds_read_b128 v[116:119], v198 offset:30720
	s_waitcnt lgkmcnt(5)
	v_mfma_scale_f32_32x32x64_f8f6f4 v[52:67], v[82:89], v[70:77], v[52:67], v188, v188 op_sel_hi:[0,0,0]
	s_waitcnt lgkmcnt(4)
	v_mfma_scale_f32_32x32x64_f8f6f4 v[36:51], v[82:89], v[90:97], v[36:51], v188, v188 op_sel_hi:[0,0,0]
	s_waitcnt lgkmcnt(1)
	v_mfma_scale_f32_32x32x64_f8f6f4 v[20:35], v[82:89], v[104:111], v[20:35], v188, v188 op_sel_hi:[0,0,0]
	s_waitcnt lgkmcnt(0)
	v_mfma_scale_f32_32x32x64_f8f6f4 v[4:19], v[82:89], v[112:119], v[4:19], v188, v188 op_sel_hi:[0,0,0]
	s_nop 0
	s_nop 15
	s_nop 15
	s_and_saveexec_b64 s[4:5], s[6:7]
	s_cbranch_execz .LBB0_386
	v_add_f32_e32 v70, v100, v101
	v_fmac_f32_e32 v70, v145, v2
	v_add_f32_e32 v2, v68, v69
	v_fmac_f32_e32 v2, v70, v102
	ds_write_b32 v184, v2
	s_branch .LBB0_386
